# speedup vs baseline: 1.0352x; 1.0102x over previous
.Lq_noearly:
	s_cmp_eq_u32 s43, 32
	s_cselect_b64 vcc, -1, 0
	v_cndmask_b32_e32 v1, v1, v139, vcc
	v_cndmask_b32_e32 v175, v175, v138, vcc
	v_mov_b32_e32 v152, 0x44800000
	v_add_u32_e32 v208, s8, v195
	v_lshl_add_u32 v155, v181, 1, v208
	v_cndmask_b32_e64 v152, v152, 0, s[4:5]
	v_fma_mixlo_f16 v153, v159, v152, 0
	v_fma_mixhi_f16 v153, v160, v152, 0
	s_cmp_lt_u32 s43, 23
	ds_write_b16 v155, v153
	ds_write_b16_d16_hi v155, v153 offset:8
	s_cbranch_scc1 .LBB1_35
	v_fma_mixlo_f16 v154, v159, v152, -v153 op_sel_hi:[0,0,1]
	v_fma_mixhi_f16 v154, v160, v152, -v153 op_sel:[0,0,1] op_sel_hi:[0,0,1]
	ds_write_b16 v155, v154 offset:8448
	ds_write_b16_d16_hi v155, v154 offset:8456

.LBB1_53:
	s_cmp_eq_u32 s44, s49
	s_waitcnt lgkmcnt(0)
	s_barrier
	s_cbranch_scc1 .LBB1_55
	s_waitcnt vmcnt(1)
	v_mov_b64_e32 v[140:141], v[136:137]
	s_waitcnt vmcnt(0)
	v_mov_b64_e32 v[144:145], v[132:133]
	s_mov_b32 s43, s44
	v_mov_b64_e32 v[138:139], v[134:135]
	v_mov_b64_e32 v[142:143], v[130:131]
	s_branch .LBB1_20
